# in-proj/gates K-loops without the per-cluster priority raise (both wave halves at priority 0)
# speedup vs baseline: 1.0054x; 1.0054x over previous
.LBB0_226:
	s_add_u32 s30, s26, 0xfffc0080
	s_addc_u32 s31, s27, -1
	s_and_b64 s[28:29], s[28:29], exec
	s_cselect_b32 s31, s21, s31
	s_cselect_b32 s30, s20, s30
	s_cselect_b32 s29, s23, s52
	s_cselect_b32 s28, s22, s49
	s_add_i32 s54, 0, 0x10000
	v_add_u32_e32 v2, s54, v163
	ds_read_b128 v[132:135], v2
	ds_read_b128 v[136:139], v2 offset:1024
	ds_read_b128 v[140:143], v2 offset:2048
	ds_read_b128 v[144:147], v2 offset:3072
	v_lshl_add_u64 v[160:161], s[26:27], 0, v[156:157]
	s_add_i32 m0, s36, 0xc000
	ds_read_b128 v[166:169], v164
	ds_read_b128 v[170:173], v164 offset:1024
	ds_read_b128 v[174:177], v164 offset:2048
	ds_read_b128 v[178:181], v164 offset:3072
	ds_read_b128 v[182:185], v164 offset:4096
	ds_read_b128 v[186:189], v164 offset:5120
	ds_read_b128 v[190:193], v164 offset:6144
	ds_read_b128 v[194:197], v164 offset:7168
	global_load_lds_dwordx4 v[160:161], off
	v_lshl_add_u64 v[160:161], s[26:27], 0, v[158:159]
	s_add_i32 m0, s36, 0xe000
	s_nop 0
	global_load_lds_dwordx4 v[160:161], off
	s_waitcnt lgkmcnt(8)
	s_barrier
	s_waitcnt lgkmcnt(0)
	s_setprio 0
	s_waitcnt lgkmcnt(0)
	v_mfma_f32_16x16x32_bf16 v[128:131], v[132:135], v[166:169], v[128:131]
	v_mfma_f32_16x16x32_bf16 v[124:127], v[140:143], v[166:169], v[124:127]
	v_mfma_f32_16x16x32_bf16 v[116:119], v[132:135], v[174:177], v[116:119]
	v_mfma_f32_16x16x32_bf16 v[108:111], v[140:143], v[174:177], v[108:111]
	v_mfma_f32_16x16x32_bf16 v[100:103], v[132:135], v[182:185], v[100:103]
	v_mfma_f32_16x16x32_bf16 v[92:95], v[140:143], v[182:185], v[92:95]
	v_mfma_f32_16x16x32_bf16 v[84:87], v[132:135], v[190:193], v[84:87]
	v_mfma_f32_16x16x32_bf16 v[76:79], v[140:143], v[190:193], v[76:79]
	v_mfma_f32_16x16x32_bf16 v[128:131], v[136:139], v[170:173], v[128:131]
	v_mfma_f32_16x16x32_bf16 v[124:127], v[144:147], v[170:173], v[124:127]
	v_mfma_f32_16x16x32_bf16 v[116:119], v[136:139], v[178:181], v[116:119]
	v_mfma_f32_16x16x32_bf16 v[108:111], v[144:147], v[178:181], v[108:111]
	v_mfma_f32_16x16x32_bf16 v[100:103], v[136:139], v[186:189], v[100:103]
	v_mfma_f32_16x16x32_bf16 v[92:95], v[144:147], v[186:189], v[92:95]
	v_mfma_f32_16x16x32_bf16 v[84:87], v[136:139], v[194:197], v[84:87]
	v_mfma_f32_16x16x32_bf16 v[76:79], v[144:147], v[194:197], v[76:79]
	s_setprio 0
	s_barrier
	s_add_i32 s56, 0, 0x14000
	s_add_i32 s54, s54, s35
	v_add_u32_e32 v2, s56, v163
	v_lshl_add_u64 v[160:161], s[28:29], 0, v[150:151]
	s_mov_b32 m0, s54
	ds_read_b128 v[198:201], v2
	ds_read_b128 v[202:205], v2 offset:1024
	ds_read_b128 v[206:209], v2 offset:2048
	ds_read_b128 v[210:213], v2 offset:3072
	global_load_lds_dwordx4 v[160:161], off
	v_lshl_add_u64 v[222:223], s[28:29], 0, v[154:155]
	s_add_i32 m0, s54, 0x2000
	s_nop 0
	global_load_lds_dwordx4 v[222:223], off
	s_barrier
	s_waitcnt lgkmcnt(0)
	s_setprio 0
	s_waitcnt lgkmcnt(0)
	v_mfma_f32_16x16x32_bf16 v[120:123], v[198:201], v[166:169], v[120:123]
	v_mfma_f32_16x16x32_bf16 v[112:115], v[206:209], v[166:169], v[112:115]
	v_mfma_f32_16x16x32_bf16 v[104:107], v[198:201], v[174:177], v[104:107]
	v_mfma_f32_16x16x32_bf16 v[96:99], v[206:209], v[174:177], v[96:99]
	v_mfma_f32_16x16x32_bf16 v[88:91], v[198:201], v[182:185], v[88:91]
	v_mfma_f32_16x16x32_bf16 v[80:83], v[206:209], v[182:185], v[80:83]
	v_mfma_f32_16x16x32_bf16 v[72:75], v[198:201], v[190:193], v[72:75]
	v_mfma_f32_16x16x32_bf16 v[68:71], v[206:209], v[190:193], v[68:71]
	v_mfma_f32_16x16x32_bf16 v[120:123], v[202:205], v[170:173], v[120:123]
	v_mfma_f32_16x16x32_bf16 v[112:115], v[210:213], v[170:173], v[112:115]
	v_mfma_f32_16x16x32_bf16 v[104:107], v[202:205], v[178:181], v[104:107]
	v_mfma_f32_16x16x32_bf16 v[96:99], v[210:213], v[178:181], v[96:99]
	v_mfma_f32_16x16x32_bf16 v[88:91], v[202:205], v[186:189], v[88:91]
	v_mfma_f32_16x16x32_bf16 v[80:83], v[210:213], v[186:189], v[80:83]
	v_mfma_f32_16x16x32_bf16 v[72:75], v[202:205], v[194:197], v[72:75]
	v_mfma_f32_16x16x32_bf16 v[68:71], v[210:213], v[194:197], v[68:71]
	s_setprio 0
	s_mov_b32 m0, s36
	v_lshl_add_u64 v[224:225], s[30:31], 0, v[148:149]
	s_barrier
	ds_read_b128 v[166:169], v164 offset:16384
	ds_read_b128 v[170:173], v164 offset:17408
	ds_read_b128 v[174:177], v164 offset:18432
	ds_read_b128 v[178:181], v164 offset:19456
	ds_read_b128 v[182:185], v164 offset:20480
	ds_read_b128 v[186:189], v164 offset:21504
	ds_read_b128 v[190:193], v164 offset:22528
	ds_read_b128 v[194:197], v164 offset:23552
	global_load_lds_dwordx4 v[224:225], off
	v_lshl_add_u64 v[230:231], s[30:31], 0, v[152:153]
	s_mov_b32 m0, s37
	s_nop 0
	global_load_lds_dwordx4 v[230:231], off
	s_barrier
	s_waitcnt lgkmcnt(0)
	s_setprio 0
	s_waitcnt lgkmcnt(0)
	v_mfma_f32_16x16x32_bf16 v[64:67], v[132:135], v[166:169], v[64:67]
	v_mfma_f32_16x16x32_bf16 v[60:63], v[140:143], v[166:169], v[60:63]
	v_mfma_f32_16x16x32_bf16 v[52:55], v[132:135], v[174:177], v[52:55]
	v_mfma_f32_16x16x32_bf16 v[44:47], v[140:143], v[174:177], v[44:47]
	v_mfma_f32_16x16x32_bf16 v[36:39], v[132:135], v[182:185], v[36:39]
	v_mfma_f32_16x16x32_bf16 v[28:31], v[140:143], v[182:185], v[28:31]
	v_mfma_f32_16x16x32_bf16 v[20:23], v[132:135], v[190:193], v[20:23]
	v_mfma_f32_16x16x32_bf16 v[12:15], v[140:143], v[190:193], v[12:15]
	v_mfma_f32_16x16x32_bf16 v[64:67], v[136:139], v[170:173], v[64:67]
	v_mfma_f32_16x16x32_bf16 v[60:63], v[144:147], v[170:173], v[60:63]
	v_mfma_f32_16x16x32_bf16 v[52:55], v[136:139], v[178:181], v[52:55]
	v_mfma_f32_16x16x32_bf16 v[44:47], v[144:147], v[178:181], v[44:47]
	v_mfma_f32_16x16x32_bf16 v[36:39], v[136:139], v[186:189], v[36:39]
	v_mfma_f32_16x16x32_bf16 v[28:31], v[144:147], v[186:189], v[28:31]
	v_mfma_f32_16x16x32_bf16 v[20:23], v[136:139], v[194:197], v[20:23]
	v_mfma_f32_16x16x32_bf16 v[12:15], v[144:147], v[194:197], v[12:15]
	s_setprio 0
	s_barrier
	s_add_u32 s54, s28, 0x40000
	s_addc_u32 s55, s29, 0
	s_add_i32 s56, s56, s35
	v_lshl_add_u64 v[132:133], s[54:55], 0, v[150:151]
	s_mov_b32 m0, s56
	s_nop 0
	global_load_lds_dwordx4 v[132:133], off
	v_lshl_add_u64 v[132:133], s[54:55], 0, v[154:155]
	s_add_i32 m0, s56, 0x2000
	s_nop 0
	global_load_lds_dwordx4 v[132:133], off
	s_waitcnt vmcnt(6)
	s_barrier
	s_setprio 0
	v_mfma_f32_16x16x32_bf16 v[56:59], v[198:201], v[166:169], v[56:59]
	v_mfma_f32_16x16x32_bf16 v[48:51], v[206:209], v[166:169], v[48:51]
	v_mfma_f32_16x16x32_bf16 v[40:43], v[198:201], v[174:177], v[40:43]
	v_mfma_f32_16x16x32_bf16 v[32:35], v[206:209], v[174:177], v[32:35]
	v_mfma_f32_16x16x32_bf16 v[24:27], v[198:201], v[182:185], v[24:27]
	v_mfma_f32_16x16x32_bf16 v[16:19], v[206:209], v[182:185], v[16:19]
	v_mfma_f32_16x16x32_bf16 v[8:11], v[198:201], v[190:193], v[8:11]
	v_mfma_f32_16x16x32_bf16 v[4:7], v[206:209], v[190:193], v[4:7]
	v_mfma_f32_16x16x32_bf16 v[56:59], v[202:205], v[170:173], v[56:59]
	v_mfma_f32_16x16x32_bf16 v[48:51], v[210:213], v[170:173], v[48:51]
	v_mfma_f32_16x16x32_bf16 v[40:43], v[202:205], v[178:181], v[40:43]
	v_mfma_f32_16x16x32_bf16 v[32:35], v[210:213], v[178:181], v[32:35]
	v_mfma_f32_16x16x32_bf16 v[24:27], v[202:205], v[186:189], v[24:27]
	v_mfma_f32_16x16x32_bf16 v[16:19], v[210:213], v[186:189], v[16:19]
	v_mfma_f32_16x16x32_bf16 v[8:11], v[202:205], v[194:197], v[8:11]
	v_mfma_f32_16x16x32_bf16 v[4:7], v[210:213], v[194:197], v[4:7]
	s_setprio 0
	s_add_i32 s54, 0, 0x18000
	v_add_u32_e32 v2, s54, v163
	s_barrier
	ds_read_b128 v[132:135], v2
	ds_read_b128 v[136:139], v2 offset:1024
	ds_read_b128 v[140:143], v2 offset:2048
	ds_read_b128 v[144:147], v2 offset:3072
	s_add_u32 s30, s30, 0x40000
	s_addc_u32 s31, s31, 0
	s_mov_b32 m0, s38
	v_lshl_add_u64 v[198:199], s[30:31], 0, v[148:149]
	ds_read_b128 v[166:169], v164 offset:32768
	ds_read_b128 v[170:173], v164 offset:33792
	ds_read_b128 v[174:177], v164 offset:34816
	ds_read_b128 v[178:181], v164 offset:35840
	ds_read_b128 v[182:185], v164 offset:36864
	ds_read_b128 v[186:189], v164 offset:37888
	ds_read_b128 v[190:193], v164 offset:38912
	ds_read_b128 v[194:197], v164 offset:39936
	global_load_lds_dwordx4 v[198:199], off
	v_lshl_add_u64 v[198:199], s[30:31], 0, v[152:153]
	s_mov_b32 m0, s39
	s_nop 0
	global_load_lds_dwordx4 v[198:199], off
	s_waitcnt lgkmcnt(8)
	s_barrier
	s_waitcnt lgkmcnt(0)
	s_setprio 0
	s_waitcnt lgkmcnt(0)
	v_mfma_f32_16x16x32_bf16 v[128:131], v[132:135], v[166:169], v[128:131]
	v_mfma_f32_16x16x32_bf16 v[124:127], v[140:143], v[166:169], v[124:127]
	v_mfma_f32_16x16x32_bf16 v[116:119], v[132:135], v[174:177], v[116:119]
	v_mfma_f32_16x16x32_bf16 v[108:111], v[140:143], v[174:177], v[108:111]
	v_mfma_f32_16x16x32_bf16 v[100:103], v[132:135], v[182:185], v[100:103]
	v_mfma_f32_16x16x32_bf16 v[92:95], v[140:143], v[182:185], v[92:95]
	v_mfma_f32_16x16x32_bf16 v[84:87], v[132:135], v[190:193], v[84:87]
	v_mfma_f32_16x16x32_bf16 v[76:79], v[140:143], v[190:193], v[76:79]
	v_mfma_f32_16x16x32_bf16 v[128:131], v[136:139], v[170:173], v[128:131]
	v_mfma_f32_16x16x32_bf16 v[124:127], v[144:147], v[170:173], v[124:127]
	v_mfma_f32_16x16x32_bf16 v[116:119], v[136:139], v[178:181], v[116:119]
	v_mfma_f32_16x16x32_bf16 v[108:111], v[144:147], v[178:181], v[108:111]
	v_mfma_f32_16x16x32_bf16 v[100:103], v[136:139], v[186:189], v[100:103]
	v_mfma_f32_16x16x32_bf16 v[92:95], v[144:147], v[186:189], v[92:95]
	v_mfma_f32_16x16x32_bf16 v[84:87], v[136:139], v[194:197], v[84:87]
	v_mfma_f32_16x16x32_bf16 v[76:79], v[144:147], v[194:197], v[76:79]
	s_setprio 0
	s_barrier
	s_add_i32 s30, 0, 0x1c000
	s_add_i32 s31, s54, s35
	v_add_u32_e32 v2, s30, v163
	v_lshl_add_u64 v[160:161], v[160:161], 0, s[60:61]
	s_mov_b32 m0, s31
	ds_read_b128 v[198:201], v2
	ds_read_b128 v[202:205], v2 offset:1024
	ds_read_b128 v[206:209], v2 offset:2048
	ds_read_b128 v[210:213], v2 offset:3072
	global_load_lds_dwordx4 v[160:161], off
	v_lshl_add_u64 v[160:161], v[222:223], 0, s[60:61]
	s_add_i32 m0, s31, 0x2000
	s_nop 0
	global_load_lds_dwordx4 v[160:161], off
	s_barrier
	s_waitcnt lgkmcnt(0)
	s_setprio 0
	s_waitcnt lgkmcnt(0)
	v_mfma_f32_16x16x32_bf16 v[120:123], v[198:201], v[166:169], v[120:123]
	v_mfma_f32_16x16x32_bf16 v[112:115], v[206:209], v[166:169], v[112:115]
	v_mfma_f32_16x16x32_bf16 v[104:107], v[198:201], v[174:177], v[104:107]
	v_mfma_f32_16x16x32_bf16 v[96:99], v[206:209], v[174:177], v[96:99]
	v_mfma_f32_16x16x32_bf16 v[88:91], v[198:201], v[182:185], v[88:91]
	v_mfma_f32_16x16x32_bf16 v[80:83], v[206:209], v[182:185], v[80:83]
	v_mfma_f32_16x16x32_bf16 v[72:75], v[198:201], v[190:193], v[72:75]
	v_mfma_f32_16x16x32_bf16 v[68:71], v[206:209], v[190:193], v[68:71]
	v_mfma_f32_16x16x32_bf16 v[120:123], v[202:205], v[170:173], v[120:123]
	v_mfma_f32_16x16x32_bf16 v[112:115], v[210:213], v[170:173], v[112:115]
	v_mfma_f32_16x16x32_bf16 v[104:107], v[202:205], v[178:181], v[104:107]
	v_mfma_f32_16x16x32_bf16 v[96:99], v[210:213], v[178:181], v[96:99]
	v_mfma_f32_16x16x32_bf16 v[88:91], v[202:205], v[186:189], v[88:91]
	v_mfma_f32_16x16x32_bf16 v[80:83], v[210:213], v[186:189], v[80:83]
	v_mfma_f32_16x16x32_bf16 v[72:75], v[202:205], v[194:197], v[72:75]
	v_mfma_f32_16x16x32_bf16 v[68:71], v[210:213], v[194:197], v[68:71]
	s_setprio 0
	s_mov_b32 m0, s42
	v_lshl_add_u64 v[160:161], v[224:225], 0, s[60:61]
	s_barrier
	ds_read_b128 v[166:169], v164 offset:49152
	ds_read_b128 v[170:173], v164 offset:50176
	ds_read_b128 v[174:177], v164 offset:51200
	ds_read_b128 v[178:181], v164 offset:52224
	ds_read_b128 v[182:185], v164 offset:53248
	ds_read_b128 v[186:189], v164 offset:54272
	ds_read_b128 v[190:193], v164 offset:55296
	ds_read_b128 v[194:197], v164 offset:56320
	global_load_lds_dwordx4 v[160:161], off
	v_lshl_add_u64 v[160:161], v[230:231], 0, s[60:61]
	s_mov_b32 m0, s43
	s_nop 0
	global_load_lds_dwordx4 v[160:161], off
	s_barrier
	s_waitcnt lgkmcnt(0)
	s_setprio 0
	s_waitcnt lgkmcnt(0)
	v_mfma_f32_16x16x32_bf16 v[64:67], v[132:135], v[166:169], v[64:67]
	v_mfma_f32_16x16x32_bf16 v[60:63], v[140:143], v[166:169], v[60:63]
	v_mfma_f32_16x16x32_bf16 v[52:55], v[132:135], v[174:177], v[52:55]
	v_mfma_f32_16x16x32_bf16 v[44:47], v[140:143], v[174:177], v[44:47]
	v_mfma_f32_16x16x32_bf16 v[36:39], v[132:135], v[182:185], v[36:39]
	v_mfma_f32_16x16x32_bf16 v[28:31], v[140:143], v[182:185], v[28:31]
	v_mfma_f32_16x16x32_bf16 v[20:23], v[132:135], v[190:193], v[20:23]
	v_mfma_f32_16x16x32_bf16 v[12:15], v[140:143], v[190:193], v[12:15]
	v_mfma_f32_16x16x32_bf16 v[64:67], v[136:139], v[170:173], v[64:67]
	v_mfma_f32_16x16x32_bf16 v[60:63], v[144:147], v[170:173], v[60:63]
	v_mfma_f32_16x16x32_bf16 v[52:55], v[136:139], v[178:181], v[52:55]
	v_mfma_f32_16x16x32_bf16 v[44:47], v[144:147], v[178:181], v[44:47]
	v_mfma_f32_16x16x32_bf16 v[36:39], v[136:139], v[186:189], v[36:39]
	v_mfma_f32_16x16x32_bf16 v[28:31], v[144:147], v[186:189], v[28:31]
	v_mfma_f32_16x16x32_bf16 v[20:23], v[136:139], v[194:197], v[20:23]
	v_mfma_f32_16x16x32_bf16 v[12:15], v[144:147], v[194:197], v[12:15]
	s_setprio 0
	s_barrier
	s_add_u32 s28, s28, 0x40080
	s_addc_u32 s29, s29, 0
	s_add_i32 s30, s30, s35
	v_lshl_add_u64 v[132:133], s[28:29], 0, v[150:151]
	s_mov_b32 m0, s30
	s_nop 0
	global_load_lds_dwordx4 v[132:133], off
	v_lshl_add_u64 v[132:133], s[28:29], 0, v[154:155]
	s_add_i32 m0, s30, 0x2000
	s_nop 0
	global_load_lds_dwordx4 v[132:133], off
	s_waitcnt vmcnt(6)
	s_barrier
	s_setprio 0
	v_mfma_f32_16x16x32_bf16 v[56:59], v[198:201], v[166:169], v[56:59]
	v_mfma_f32_16x16x32_bf16 v[48:51], v[206:209], v[166:169], v[48:51]
	v_mfma_f32_16x16x32_bf16 v[40:43], v[198:201], v[174:177], v[40:43]
	v_mfma_f32_16x16x32_bf16 v[32:35], v[206:209], v[174:177], v[32:35]
	v_mfma_f32_16x16x32_bf16 v[24:27], v[198:201], v[182:185], v[24:27]
	v_mfma_f32_16x16x32_bf16 v[16:19], v[206:209], v[182:185], v[16:19]
	v_mfma_f32_16x16x32_bf16 v[8:11], v[198:201], v[190:193], v[8:11]
	v_mfma_f32_16x16x32_bf16 v[4:7], v[206:209], v[190:193], v[4:7]
	v_mfma_f32_16x16x32_bf16 v[56:59], v[202:205], v[170:173], v[56:59]
	v_mfma_f32_16x16x32_bf16 v[48:51], v[210:213], v[170:173], v[48:51]
	v_mfma_f32_16x16x32_bf16 v[40:43], v[202:205], v[178:181], v[40:43]
	v_mfma_f32_16x16x32_bf16 v[32:35], v[210:213], v[178:181], v[32:35]
	v_mfma_f32_16x16x32_bf16 v[24:27], v[202:205], v[186:189], v[24:27]
	v_mfma_f32_16x16x32_bf16 v[16:19], v[210:213], v[186:189], v[16:19]
	v_mfma_f32_16x16x32_bf16 v[8:11], v[202:205], v[194:197], v[8:11]
	v_mfma_f32_16x16x32_bf16 v[4:7], v[210:213], v[194:197], v[4:7]
	s_setprio 0
	s_add_i32 s53, s53, 2
	s_add_u32 s26, s26, 0x100
	s_addc_u32 s27, s27, 0
	s_add_u32 s49, s49, 0x100
	s_addc_u32 s52, s52, 0
	s_cmp_gt_u32 s53, 13
	s_barrier
	s_cbranch_scc1 .LBB0_230

.Lmy_bias_skip:
	s_add_u32 s38, s34, 0xfffc0080
	s_addc_u32 s39, s35, -1
	s_and_b64 s[36:37], s[36:37], exec
	s_cselect_b32 s39, s27, s39
	s_cselect_b32 s38, s26, s38
	s_cselect_b32 s37, s29, s63
	s_cselect_b32 s36, s28, s62
	s_add_i32 s65, 0, 0x10000
	v_add_u32_e32 v2, s65, v163
	ds_read_b128 v[132:135], v2
	ds_read_b128 v[136:139], v2 offset:1024
	ds_read_b128 v[140:143], v2 offset:2048
	ds_read_b128 v[144:147], v2 offset:3072
	v_lshl_add_u64 v[160:161], s[34:35], 0, v[156:157]
	s_add_i32 m0, s42, 0xc000
	ds_read_b128 v[166:169], v164
	ds_read_b128 v[170:173], v164 offset:1024
	ds_read_b128 v[174:177], v164 offset:2048
	ds_read_b128 v[178:181], v164 offset:3072
	ds_read_b128 v[182:185], v164 offset:4096
	ds_read_b128 v[186:189], v164 offset:5120
	ds_read_b128 v[190:193], v164 offset:6144
	ds_read_b128 v[194:197], v164 offset:7168
	global_load_lds_dwordx4 v[160:161], off
	v_lshl_add_u64 v[160:161], s[34:35], 0, v[158:159]
	s_add_i32 m0, s42, 0xe000
	s_nop 0
	global_load_lds_dwordx4 v[160:161], off
	s_waitcnt lgkmcnt(8)
	s_barrier
	s_waitcnt lgkmcnt(0)
	s_setprio 0
	s_waitcnt lgkmcnt(0)
	v_mfma_f32_16x16x32_bf16 v[128:131], v[132:135], v[166:169], v[128:131]
	v_mfma_f32_16x16x32_bf16 v[124:127], v[140:143], v[166:169], v[124:127]
	v_mfma_f32_16x16x32_bf16 v[112:115], v[132:135], v[174:177], v[112:115]
	v_mfma_f32_16x16x32_bf16 v[108:111], v[140:143], v[174:177], v[108:111]
	v_mfma_f32_16x16x32_bf16 v[96:99], v[132:135], v[182:185], v[96:99]
	v_mfma_f32_16x16x32_bf16 v[92:95], v[140:143], v[182:185], v[92:95]
	v_mfma_f32_16x16x32_bf16 v[80:83], v[132:135], v[190:193], v[80:83]
	v_mfma_f32_16x16x32_bf16 v[76:79], v[140:143], v[190:193], v[76:79]
	v_mfma_f32_16x16x32_bf16 v[128:131], v[136:139], v[170:173], v[128:131]
	v_mfma_f32_16x16x32_bf16 v[124:127], v[144:147], v[170:173], v[124:127]
	v_mfma_f32_16x16x32_bf16 v[112:115], v[136:139], v[178:181], v[112:115]
	v_mfma_f32_16x16x32_bf16 v[108:111], v[144:147], v[178:181], v[108:111]
	v_mfma_f32_16x16x32_bf16 v[96:99], v[136:139], v[186:189], v[96:99]
	v_mfma_f32_16x16x32_bf16 v[92:95], v[144:147], v[186:189], v[92:95]
	v_mfma_f32_16x16x32_bf16 v[80:83], v[136:139], v[194:197], v[80:83]
	v_mfma_f32_16x16x32_bf16 v[76:79], v[144:147], v[194:197], v[76:79]
	s_setprio 0
	s_barrier
	s_add_i32 s68, 0, 0x14000
	s_add_i32 s65, s65, s41
	v_add_u32_e32 v2, s68, v163
	v_lshl_add_u64 v[160:161], s[36:37], 0, v[150:151]
	s_mov_b32 m0, s65
	ds_read_b128 v[198:201], v2
	ds_read_b128 v[202:205], v2 offset:1024
	ds_read_b128 v[206:209], v2 offset:2048
	ds_read_b128 v[210:213], v2 offset:3072
	global_load_lds_dwordx4 v[160:161], off
	v_lshl_add_u64 v[222:223], s[36:37], 0, v[154:155]
	s_add_i32 m0, s65, 0x2000
	s_nop 0
	global_load_lds_dwordx4 v[222:223], off
	s_barrier
	s_waitcnt lgkmcnt(0)
	s_setprio 0
	s_waitcnt lgkmcnt(0)
	v_mfma_f32_16x16x32_bf16 v[120:123], v[198:201], v[166:169], v[120:123]
	v_mfma_f32_16x16x32_bf16 v[116:119], v[206:209], v[166:169], v[116:119]
	v_mfma_f32_16x16x32_bf16 v[104:107], v[198:201], v[174:177], v[104:107]
	v_mfma_f32_16x16x32_bf16 v[100:103], v[206:209], v[174:177], v[100:103]
	v_mfma_f32_16x16x32_bf16 v[88:91], v[198:201], v[182:185], v[88:91]
	v_mfma_f32_16x16x32_bf16 v[84:87], v[206:209], v[182:185], v[84:87]
	v_mfma_f32_16x16x32_bf16 v[72:75], v[198:201], v[190:193], v[72:75]
	v_mfma_f32_16x16x32_bf16 v[68:71], v[206:209], v[190:193], v[68:71]
	v_mfma_f32_16x16x32_bf16 v[120:123], v[202:205], v[170:173], v[120:123]
	v_mfma_f32_16x16x32_bf16 v[116:119], v[210:213], v[170:173], v[116:119]
	v_mfma_f32_16x16x32_bf16 v[104:107], v[202:205], v[178:181], v[104:107]
	v_mfma_f32_16x16x32_bf16 v[100:103], v[210:213], v[178:181], v[100:103]
	v_mfma_f32_16x16x32_bf16 v[88:91], v[202:205], v[186:189], v[88:91]
	v_mfma_f32_16x16x32_bf16 v[84:87], v[210:213], v[186:189], v[84:87]
	v_mfma_f32_16x16x32_bf16 v[72:75], v[202:205], v[194:197], v[72:75]
	v_mfma_f32_16x16x32_bf16 v[68:71], v[210:213], v[194:197], v[68:71]
	s_setprio 0
	s_mov_b32 m0, s42
	v_lshl_add_u64 v[224:225], s[38:39], 0, v[148:149]
	s_barrier
	ds_read_b128 v[166:169], v164 offset:16384
	ds_read_b128 v[170:173], v164 offset:17408
	ds_read_b128 v[174:177], v164 offset:18432
	ds_read_b128 v[178:181], v164 offset:19456
	ds_read_b128 v[182:185], v164 offset:20480
	ds_read_b128 v[186:189], v164 offset:21504
	ds_read_b128 v[190:193], v164 offset:22528
	ds_read_b128 v[194:197], v164 offset:23552
	global_load_lds_dwordx4 v[224:225], off
	v_lshl_add_u64 v[230:231], s[38:39], 0, v[152:153]
	s_mov_b32 m0, s43
	s_nop 0
	global_load_lds_dwordx4 v[230:231], off
	s_barrier
	s_waitcnt lgkmcnt(0)
	s_setprio 0
	s_waitcnt lgkmcnt(0)
	v_mfma_f32_16x16x32_bf16 v[64:67], v[132:135], v[166:169], v[64:67]
	v_mfma_f32_16x16x32_bf16 v[60:63], v[140:143], v[166:169], v[60:63]
	v_mfma_f32_16x16x32_bf16 v[48:51], v[132:135], v[174:177], v[48:51]
	v_mfma_f32_16x16x32_bf16 v[44:47], v[140:143], v[174:177], v[44:47]
	v_mfma_f32_16x16x32_bf16 v[32:35], v[132:135], v[182:185], v[32:35]
	v_mfma_f32_16x16x32_bf16 v[28:31], v[140:143], v[182:185], v[28:31]
	v_mfma_f32_16x16x32_bf16 v[16:19], v[132:135], v[190:193], v[16:19]
	v_mfma_f32_16x16x32_bf16 v[12:15], v[140:143], v[190:193], v[12:15]
	v_mfma_f32_16x16x32_bf16 v[64:67], v[136:139], v[170:173], v[64:67]
	v_mfma_f32_16x16x32_bf16 v[60:63], v[144:147], v[170:173], v[60:63]
	v_mfma_f32_16x16x32_bf16 v[48:51], v[136:139], v[178:181], v[48:51]
	v_mfma_f32_16x16x32_bf16 v[44:47], v[144:147], v[178:181], v[44:47]
	v_mfma_f32_16x16x32_bf16 v[32:35], v[136:139], v[186:189], v[32:35]
	v_mfma_f32_16x16x32_bf16 v[28:31], v[144:147], v[186:189], v[28:31]
	v_mfma_f32_16x16x32_bf16 v[16:19], v[136:139], v[194:197], v[16:19]
	v_mfma_f32_16x16x32_bf16 v[12:15], v[144:147], v[194:197], v[12:15]
	s_setprio 0
	s_barrier
	s_add_u32 s66, s36, 0x40000
	s_addc_u32 s67, s37, 0
	s_add_i32 s65, s68, s41
	v_lshl_add_u64 v[132:133], s[66:67], 0, v[150:151]
	s_mov_b32 m0, s65
	s_nop 0
	global_load_lds_dwordx4 v[132:133], off
	v_lshl_add_u64 v[132:133], s[66:67], 0, v[154:155]
	s_add_i32 m0, s65, 0x2000
	s_nop 0
	global_load_lds_dwordx4 v[132:133], off
	s_waitcnt vmcnt(6)
	s_barrier
	s_setprio 0
	v_mfma_f32_16x16x32_bf16 v[56:59], v[198:201], v[166:169], v[56:59]
	v_mfma_f32_16x16x32_bf16 v[52:55], v[206:209], v[166:169], v[52:55]
	v_mfma_f32_16x16x32_bf16 v[40:43], v[198:201], v[174:177], v[40:43]
	v_mfma_f32_16x16x32_bf16 v[36:39], v[206:209], v[174:177], v[36:39]
	v_mfma_f32_16x16x32_bf16 v[24:27], v[198:201], v[182:185], v[24:27]
	v_mfma_f32_16x16x32_bf16 v[20:23], v[206:209], v[182:185], v[20:23]
	v_mfma_f32_16x16x32_bf16 v[8:11], v[198:201], v[190:193], v[8:11]
	v_mfma_f32_16x16x32_bf16 v[4:7], v[206:209], v[190:193], v[4:7]
	v_mfma_f32_16x16x32_bf16 v[56:59], v[202:205], v[170:173], v[56:59]
	v_mfma_f32_16x16x32_bf16 v[52:55], v[210:213], v[170:173], v[52:55]
	v_mfma_f32_16x16x32_bf16 v[40:43], v[202:205], v[178:181], v[40:43]
	v_mfma_f32_16x16x32_bf16 v[36:39], v[210:213], v[178:181], v[36:39]
	v_mfma_f32_16x16x32_bf16 v[24:27], v[202:205], v[186:189], v[24:27]
	v_mfma_f32_16x16x32_bf16 v[20:23], v[210:213], v[186:189], v[20:23]
	v_mfma_f32_16x16x32_bf16 v[8:11], v[202:205], v[194:197], v[8:11]
	v_mfma_f32_16x16x32_bf16 v[4:7], v[210:213], v[194:197], v[4:7]
	s_setprio 0
	s_add_i32 s65, 0, 0x18000
	v_add_u32_e32 v2, s65, v163
	s_barrier
	ds_read_b128 v[132:135], v2
	ds_read_b128 v[136:139], v2 offset:1024
	ds_read_b128 v[140:143], v2 offset:2048
	ds_read_b128 v[144:147], v2 offset:3072
	s_add_u32 s38, s38, 0x40000
	s_addc_u32 s39, s39, 0
	s_mov_b32 m0, s44
	v_lshl_add_u64 v[198:199], s[38:39], 0, v[148:149]
	ds_read_b128 v[166:169], v164 offset:32768
	ds_read_b128 v[170:173], v164 offset:33792
	ds_read_b128 v[174:177], v164 offset:34816
	ds_read_b128 v[178:181], v164 offset:35840
	ds_read_b128 v[182:185], v164 offset:36864
	ds_read_b128 v[186:189], v164 offset:37888
	ds_read_b128 v[190:193], v164 offset:38912
	ds_read_b128 v[194:197], v164 offset:39936
	global_load_lds_dwordx4 v[198:199], off
	v_lshl_add_u64 v[198:199], s[38:39], 0, v[152:153]
	s_mov_b32 m0, s45
	s_nop 0
	global_load_lds_dwordx4 v[198:199], off
	s_waitcnt lgkmcnt(8)
	s_barrier
	s_waitcnt lgkmcnt(0)
	s_setprio 0
	s_waitcnt lgkmcnt(0)
	v_mfma_f32_16x16x32_bf16 v[128:131], v[132:135], v[166:169], v[128:131]
	v_mfma_f32_16x16x32_bf16 v[124:127], v[140:143], v[166:169], v[124:127]
	v_mfma_f32_16x16x32_bf16 v[112:115], v[132:135], v[174:177], v[112:115]
	v_mfma_f32_16x16x32_bf16 v[108:111], v[140:143], v[174:177], v[108:111]
	v_mfma_f32_16x16x32_bf16 v[96:99], v[132:135], v[182:185], v[96:99]
	v_mfma_f32_16x16x32_bf16 v[92:95], v[140:143], v[182:185], v[92:95]
	v_mfma_f32_16x16x32_bf16 v[80:83], v[132:135], v[190:193], v[80:83]
	v_mfma_f32_16x16x32_bf16 v[76:79], v[140:143], v[190:193], v[76:79]
	v_mfma_f32_16x16x32_bf16 v[128:131], v[136:139], v[170:173], v[128:131]
	v_mfma_f32_16x16x32_bf16 v[124:127], v[144:147], v[170:173], v[124:127]
	v_mfma_f32_16x16x32_bf16 v[112:115], v[136:139], v[178:181], v[112:115]
	v_mfma_f32_16x16x32_bf16 v[108:111], v[144:147], v[178:181], v[108:111]
	v_mfma_f32_16x16x32_bf16 v[96:99], v[136:139], v[186:189], v[96:99]
	v_mfma_f32_16x16x32_bf16 v[92:95], v[144:147], v[186:189], v[92:95]
	v_mfma_f32_16x16x32_bf16 v[80:83], v[136:139], v[194:197], v[80:83]
	v_mfma_f32_16x16x32_bf16 v[76:79], v[144:147], v[194:197], v[76:79]
	s_setprio 0
	s_barrier
	s_add_i32 s38, 0, 0x1c000
	s_add_i32 s39, s65, s41
	v_add_u32_e32 v2, s38, v163
	v_lshl_add_u64 v[160:161], v[160:161], 0, s[60:61]
	s_mov_b32 m0, s39
	ds_read_b128 v[198:201], v2
	ds_read_b128 v[202:205], v2 offset:1024
	ds_read_b128 v[206:209], v2 offset:2048
	ds_read_b128 v[210:213], v2 offset:3072
	global_load_lds_dwordx4 v[160:161], off
	v_lshl_add_u64 v[160:161], v[222:223], 0, s[60:61]
	s_add_i32 m0, s39, 0x2000
	s_nop 0
	global_load_lds_dwordx4 v[160:161], off
	s_barrier
	s_waitcnt lgkmcnt(0)
	s_setprio 0
	s_waitcnt lgkmcnt(0)
	v_mfma_f32_16x16x32_bf16 v[120:123], v[198:201], v[166:169], v[120:123]
	v_mfma_f32_16x16x32_bf16 v[116:119], v[206:209], v[166:169], v[116:119]
	v_mfma_f32_16x16x32_bf16 v[104:107], v[198:201], v[174:177], v[104:107]
	v_mfma_f32_16x16x32_bf16 v[100:103], v[206:209], v[174:177], v[100:103]
	v_mfma_f32_16x16x32_bf16 v[88:91], v[198:201], v[182:185], v[88:91]
	v_mfma_f32_16x16x32_bf16 v[84:87], v[206:209], v[182:185], v[84:87]
	v_mfma_f32_16x16x32_bf16 v[72:75], v[198:201], v[190:193], v[72:75]
	v_mfma_f32_16x16x32_bf16 v[68:71], v[206:209], v[190:193], v[68:71]
	v_mfma_f32_16x16x32_bf16 v[120:123], v[202:205], v[170:173], v[120:123]
	v_mfma_f32_16x16x32_bf16 v[116:119], v[210:213], v[170:173], v[116:119]
	v_mfma_f32_16x16x32_bf16 v[104:107], v[202:205], v[178:181], v[104:107]
	v_mfma_f32_16x16x32_bf16 v[100:103], v[210:213], v[178:181], v[100:103]
	v_mfma_f32_16x16x32_bf16 v[88:91], v[202:205], v[186:189], v[88:91]
	v_mfma_f32_16x16x32_bf16 v[84:87], v[210:213], v[186:189], v[84:87]
	v_mfma_f32_16x16x32_bf16 v[72:75], v[202:205], v[194:197], v[72:75]
	v_mfma_f32_16x16x32_bf16 v[68:71], v[210:213], v[194:197], v[68:71]
	s_setprio 0
	s_mov_b32 m0, s48
	v_lshl_add_u64 v[160:161], v[224:225], 0, s[60:61]
	s_barrier
	ds_read_b128 v[166:169], v164 offset:49152
	ds_read_b128 v[170:173], v164 offset:50176
	ds_read_b128 v[174:177], v164 offset:51200
	ds_read_b128 v[178:181], v164 offset:52224
	ds_read_b128 v[182:185], v164 offset:53248
	ds_read_b128 v[186:189], v164 offset:54272
	ds_read_b128 v[190:193], v164 offset:55296
	ds_read_b128 v[194:197], v164 offset:56320
	global_load_lds_dwordx4 v[160:161], off
	v_lshl_add_u64 v[160:161], v[230:231], 0, s[60:61]
	s_mov_b32 m0, s49
	s_nop 0
	global_load_lds_dwordx4 v[160:161], off
	s_barrier
	s_waitcnt lgkmcnt(0)
	s_setprio 0
	s_waitcnt lgkmcnt(0)
	v_mfma_f32_16x16x32_bf16 v[64:67], v[132:135], v[166:169], v[64:67]
	v_mfma_f32_16x16x32_bf16 v[60:63], v[140:143], v[166:169], v[60:63]
	v_mfma_f32_16x16x32_bf16 v[48:51], v[132:135], v[174:177], v[48:51]
	v_mfma_f32_16x16x32_bf16 v[44:47], v[140:143], v[174:177], v[44:47]
	v_mfma_f32_16x16x32_bf16 v[32:35], v[132:135], v[182:185], v[32:35]
	v_mfma_f32_16x16x32_bf16 v[28:31], v[140:143], v[182:185], v[28:31]
	v_mfma_f32_16x16x32_bf16 v[16:19], v[132:135], v[190:193], v[16:19]
	v_mfma_f32_16x16x32_bf16 v[12:15], v[140:143], v[190:193], v[12:15]
	v_mfma_f32_16x16x32_bf16 v[64:67], v[136:139], v[170:173], v[64:67]
	v_mfma_f32_16x16x32_bf16 v[60:63], v[144:147], v[170:173], v[60:63]
	v_mfma_f32_16x16x32_bf16 v[48:51], v[136:139], v[178:181], v[48:51]
	v_mfma_f32_16x16x32_bf16 v[44:47], v[144:147], v[178:181], v[44:47]
	v_mfma_f32_16x16x32_bf16 v[32:35], v[136:139], v[186:189], v[32:35]
	v_mfma_f32_16x16x32_bf16 v[28:31], v[144:147], v[186:189], v[28:31]
	v_mfma_f32_16x16x32_bf16 v[16:19], v[136:139], v[194:197], v[16:19]
	v_mfma_f32_16x16x32_bf16 v[12:15], v[144:147], v[194:197], v[12:15]
	s_setprio 0
	s_barrier
	s_add_u32 s36, s36, 0x40080
	s_addc_u32 s37, s37, 0
	s_add_i32 s38, s38, s41
	v_lshl_add_u64 v[132:133], s[36:37], 0, v[150:151]
	s_mov_b32 m0, s38
	s_nop 0
	global_load_lds_dwordx4 v[132:133], off
	v_lshl_add_u64 v[132:133], s[36:37], 0, v[154:155]
	s_add_i32 m0, s38, 0x2000
	s_nop 0
	global_load_lds_dwordx4 v[132:133], off
	s_waitcnt vmcnt(6)
	s_barrier
	s_setprio 0
	v_mfma_f32_16x16x32_bf16 v[56:59], v[198:201], v[166:169], v[56:59]
	v_mfma_f32_16x16x32_bf16 v[52:55], v[206:209], v[166:169], v[52:55]
	v_mfma_f32_16x16x32_bf16 v[40:43], v[198:201], v[174:177], v[40:43]
	v_mfma_f32_16x16x32_bf16 v[36:39], v[206:209], v[174:177], v[36:39]
	v_mfma_f32_16x16x32_bf16 v[24:27], v[198:201], v[182:185], v[24:27]
	v_mfma_f32_16x16x32_bf16 v[20:23], v[206:209], v[182:185], v[20:23]
	v_mfma_f32_16x16x32_bf16 v[8:11], v[198:201], v[190:193], v[8:11]
	v_mfma_f32_16x16x32_bf16 v[4:7], v[206:209], v[190:193], v[4:7]
	v_mfma_f32_16x16x32_bf16 v[56:59], v[202:205], v[170:173], v[56:59]
	v_mfma_f32_16x16x32_bf16 v[52:55], v[210:213], v[170:173], v[52:55]
	v_mfma_f32_16x16x32_bf16 v[40:43], v[202:205], v[178:181], v[40:43]
	v_mfma_f32_16x16x32_bf16 v[36:39], v[210:213], v[178:181], v[36:39]
	v_mfma_f32_16x16x32_bf16 v[24:27], v[202:205], v[186:189], v[24:27]
	v_mfma_f32_16x16x32_bf16 v[20:23], v[210:213], v[186:189], v[20:23]
	v_mfma_f32_16x16x32_bf16 v[8:11], v[202:205], v[194:197], v[8:11]
	v_mfma_f32_16x16x32_bf16 v[4:7], v[210:213], v[194:197], v[4:7]
	s_setprio 0
	s_add_i32 s64, s64, 2
	s_add_u32 s34, s34, 0x100
	s_addc_u32 s35, s35, 0
	s_add_u32 s62, s62, 0x100
	s_addc_u32 s63, s63, 0
	s_cmp_gt_u32 s64, 13
	s_barrier
	s_cbranch_scc1 .LBB0_1981
